# MLA QK^T phase: no softmax VALU in the first three MFMA gaps behind the step barrier; add/pack/V-read/exp2 stream re-dealt over gaps 4-12
# baseline (speedup 1.0000x reference)
.LBB0_1149:
	s_setprio 1
	s_waitcnt lgkmcnt(0)
	v_mfma_f32_32x32x16_bf16 v[100:115], v[202:205], v[136:139], v[36:51]
	s_add_i32 s19, s27, -1
	s_and_b32 s18, s19, 3
	s_mul_i32 s20, s18, 0x3000
	s_and_b32 s17, s14, 0x6000
	s_add_i32 s16, s27, 2
	s_min_i32 s8, s16, s2
	s_lshl_b64 s[10:11], s[8:9], 17
	v_lshl_add_u64 v[154:155], v[176:177], 0, s[10:11]
	s_and_b32 s10, s16, 3
	s_mulk_i32 s10, 0x3000
	s_add_i32 s10, s26, s10
	s_mov_b32 m0, s10
	s_nop 0
	global_load_lds_dwordx4 v[154:155], off
	ds_read_b128 v[202:205], v156 offset:4096
	v_mfma_f32_32x32x16_bf16 v[84:99], v[190:193], v[136:139], v[36:51]
	s_and_b64 vcc, exec, s[38:39]
	s_cbranch_vccnz .Lmla_rope1
	s_lshl_b64 s[12:13], s[8:9], 18
	v_lshl_add_u64 v[154:155], v[180:181], 0, s[12:13]
	s_add_i32 m0, s10, 0x2000
	s_nop 0
	global_load_lds_dwordx4 v[154:155], off
.Lmla_rope1:
	ds_read_b128 v[190:193], v156 offset:4608
	v_mfma_f32_32x32x16_bf16 v[100:115], v[194:197], v[132:135], v[100:115]
	s_add_i32 s8, s27, 1
	s_min_i32 s8, s8, s2
	s_lshl_b32 s8, s8, 17
	v_lshl_add_u64 v[154:155], v[178:179], 0, s[8:9]
	s_add_i32 s8, s14, 0xffffe000
	s_and_b32 s15, s8, 0x6000
	s_add_i32 s8, s26, s15
	v_lshl_add_u64 v[154:155], v[154:155], 0, s[24:25]
	s_add_i32 m0, s8, 0xc000
	s_nop 0
	global_load_lds_dwordx4 v[154:155], off
	ds_read_b128 v[194:197], v156 offset:6144
	v_mfma_f32_32x32x16_bf16 v[84:99], v[198:201], v[132:135], v[84:99]
	ds_read_b128 v[198:201], v156 offset:6656
	v_exp_f32_e32 v60, v60
	v_exp_f32_e32 v61, v61
	v_exp_f32_e32 v62, v62
	v_exp_f32_e32 v63, v63
	s_waitcnt lgkmcnt(0)
	v_mfma_f32_32x32x16_bf16 v[100:115], v[202:205], v[128:131], v[100:115]
	ds_read_b128 v[202:205], v156 offset:8192
	v_exp_f32_e32 v64, v64
	v_exp_f32_e32 v65, v65
	v_exp_f32_e32 v66, v66
	v_exp_f32_e32 v67, v67
	v_mfma_f32_32x32x16_bf16 v[84:99], v[190:193], v[128:131], v[84:99]
	ds_read_b128 v[190:193], v156 offset:8704
	v_add_f32_e32 v162, v68, v69
	ds_read_b64_tr_b16 v[172:173], v157 offset:49152
	ds_read_b64_tr_b16 v[174:175], v157 offset:49664
	v_add_f32_e32 v161, v70, v162
	v_add_f32_e32 v161, v71, v161
	v_add_f32_e32 v161, v72, v161
	v_add_f32_e32 v144, v73, v161
	v_cvt_pk_bf16_f32 v140, v68, v69
	v_mfma_f32_32x32x16_bf16 v[100:115], v[194:197], v[124:127], v[100:115]
	ds_read_b128 v[194:197], v156 offset:10240
	v_cvt_pk_bf16_f32 v141, v70, v71
	ds_read_b64_tr_b16 v[68:69], v157 offset:53248
	ds_read_b64_tr_b16 v[70:71], v157 offset:53760
	v_add_f32_e32 v142, v74, v144
	v_add_f32_e32 v142, v75, v142
	v_add_f32_e32 v142, v76, v142
	v_add_f32_e32 v144, v77, v142
	v_cvt_pk_bf16_f32 v142, v72, v73
	v_mfma_f32_32x32x16_bf16 v[84:99], v[198:201], v[124:127], v[84:99]
	ds_read_b128 v[198:201], v156 offset:10752
	v_cvt_pk_bf16_f32 v143, v74, v75
	ds_read_b64_tr_b16 v[72:73], v157 offset:50176
	ds_read_b64_tr_b16 v[74:75], v157 offset:50688
	v_add_f32_e32 v144, v78, v144
	v_add_f32_e32 v144, v79, v144
	v_add_f32_e32 v144, v80, v144
	v_add_f32_e32 v148, v81, v144
	v_cvt_pk_bf16_f32 v144, v76, v77
	s_waitcnt lgkmcnt(0)
	v_mfma_f32_32x32x16_bf16 v[100:115], v[202:205], v[120:123], v[100:115]
	v_cvt_pk_bf16_f32 v145, v78, v79
	ds_read_b64_tr_b16 v[76:77], v157 offset:54272
	ds_read_b64_tr_b16 v[78:79], v157 offset:54784
	v_add_f32_e32 v146, v82, v148
	v_add_f32_e32 v146, v83, v146
	v_add_f32_e32 v146, v52, v146
	v_add_f32_e32 v148, v53, v146
	v_cvt_pk_bf16_f32 v146, v80, v81
	v_cvt_pk_bf16_f32 v147, v82, v83
	ds_read_b64_tr_b16 v[80:81], v157 offset:51200
	v_mfma_f32_32x32x16_bf16 v[84:99], v[190:193], v[120:123], v[84:99]
	ds_read_b64_tr_b16 v[82:83], v157 offset:51712
	v_add_f32_e32 v148, v54, v148
	v_add_f32_e32 v148, v55, v148
	v_add_f32_e32 v148, v56, v148
	v_add_f32_e32 v152, v57, v148
	v_cvt_pk_bf16_f32 v148, v52, v53
	v_cvt_pk_bf16_f32 v149, v54, v55
	ds_read_b64_tr_b16 v[52:53], v157 offset:55296
	ds_read_b64_tr_b16 v[54:55], v157 offset:55808
	v_add_f32_e32 v150, v58, v152
	v_mfma_f32_32x32x16_bf16 v[100:115], v[194:197], v[116:119], v[100:115]
	v_add_f32_e32 v150, v59, v150
	v_add_f32_e32 v150, v60, v150
	v_add_f32_e32 v152, v61, v150
	v_cvt_pk_bf16_f32 v150, v56, v57
	v_cvt_pk_bf16_f32 v151, v58, v59
	ds_read_b64_tr_b16 v[56:57], v157 offset:52224
	ds_read_b64_tr_b16 v[58:59], v157 offset:52736
	v_add_f32_e32 v152, v62, v152
	v_add_f32_e32 v152, v63, v152
	v_add_f32_e32 v152, v64, v152
	v_mfma_f32_32x32x16_bf16 v[84:99], v[198:201], v[116:119], v[84:99]
	v_add_f32_e32 v160, v65, v152
	v_cvt_pk_bf16_f32 v152, v60, v61
	v_cvt_pk_bf16_f32 v153, v62, v63
	ds_read_b64_tr_b16 v[60:61], v157 offset:56320
	ds_read_b64_tr_b16 v[62:63], v157 offset:56832
	v_add_f32_e32 v154, v66, v160
	v_add_f32_e32 v156, v67, v154
	v_cvt_pk_bf16_f32 v154, v64, v65
	v_cvt_pk_bf16_f32 v155, v66, v67
	s_setprio 0
	s_cmp_lt_i32 s19, s52
	s_cbranch_scc0 .LBB0_1167

.LBB0_1153:
	s_waitcnt lgkmcnt(0)
	v_mfma_f32_32x32x16_bf16 v[4:19], v[140:143], v[172:175], v[4:19]
	v_exp_f32_e32 v100, v100
	v_exp_f32_e32 v101, v101
	v_exp_f32_e32 v102, v102
	v_exp_f32_e32 v103, v103
	v_mfma_f32_32x32x16_bf16 v[20:35], v[140:143], v[68:71], v[20:35]
	v_exp_f32_e32 v104, v104
	v_exp_f32_e32 v105, v105
	v_exp_f32_e32 v106, v106
	v_exp_f32_e32 v107, v107
	s_and_b32 s12, s27, 3
	s_mulk_i32 s12, 0x3000
	v_add_u32_e32 v140, s12, v188
	v_lshl_add_u32 v141, s18, 13, v186
	ds_read_b128 v[202:205], v140
	ds_read_b128 v[190:193], v140 offset:512
	ds_read_b128 v[194:197], v140 offset:2048
	ds_read_b128 v[198:201], v140 offset:2560
	v_mfma_f32_32x32x16_bf16 v[4:19], v[144:147], v[72:75], v[4:19]
	v_exp_f32_e32 v108, v108
	v_exp_f32_e32 v109, v109
	v_exp_f32_e32 v110, v110
	v_exp_f32_e32 v111, v111
	v_mfma_f32_32x32x16_bf16 v[20:35], v[144:147], v[76:79], v[20:35]
	v_exp_f32_e32 v112, v112
	v_exp_f32_e32 v113, v113
	v_exp_f32_e32 v114, v114
	v_exp_f32_e32 v115, v115
	v_mfma_f32_32x32x16_bf16 v[4:19], v[148:151], v[80:83], v[4:19]
	v_exp_f32_e32 v84, v84
	v_exp_f32_e32 v85, v85
	v_exp_f32_e32 v86, v86
	v_exp_f32_e32 v87, v87
	v_mfma_f32_32x32x16_bf16 v[20:35], v[148:151], v[52:55], v[20:35]
	v_exp_f32_e32 v88, v88
	v_exp_f32_e32 v89, v89
	v_exp_f32_e32 v90, v90
	v_exp_f32_e32 v91, v91
	v_mfma_f32_32x32x16_bf16 v[4:19], v[152:155], v[56:59], v[4:19]
	v_mfma_f32_32x32x16_bf16 v[20:35], v[152:155], v[60:63], v[20:35]
	s_and_b64 vcc, exec, s[10:11]
	s_cbranch_vccnz .Lmla_resc1

.LBB0_1159:
	s_setprio 1
	s_waitcnt lgkmcnt(0)
	v_mfma_f32_32x32x16_bf16 v[68:83], v[202:205], v[136:139], v[36:51]
	s_add_i32 s8, s27, 3
	s_min_i32 s8, s8, s2
	s_lshl_b64 s[10:11], s[8:9], 17
	v_lshl_add_u64 v[170:171], v[176:177], 0, s[10:11]
	s_add_i32 s10, s26, s20
	s_mov_b32 m0, s10
	s_nop 0
	global_load_lds_dwordx4 v[170:171], off
	ds_read_b128 v[202:205], v140 offset:4096
	v_mfma_f32_32x32x16_bf16 v[52:67], v[190:193], v[136:139], v[36:51]
	s_and_b64 vcc, exec, s[38:39]
	s_cbranch_vccnz .Lmla_rope2
	s_lshl_b64 s[12:13], s[8:9], 18
	v_lshl_add_u64 v[170:171], v[180:181], 0, s[12:13]
	s_add_i32 m0, s10, 0x2000
	s_nop 0
	global_load_lds_dwordx4 v[170:171], off
.Lmla_rope2:
	ds_read_b128 v[190:193], v140 offset:4608
	v_mfma_f32_32x32x16_bf16 v[68:83], v[194:197], v[132:135], v[68:83]
	s_cmp_lt_u32 s19, s3
	s_cselect_b32 s8, s16, s2
	s_lshl_b64 s[10:11], s[8:9], 17
	v_lshl_add_u64 v[170:171], v[178:179], 0, s[10:11]
	s_add_i32 s8, s26, s17
	v_lshl_add_u64 v[170:171], v[170:171], 0, s[24:25]
	s_add_i32 m0, s8, 0xc000
	s_and_b32 s17, s27, 3
	global_load_lds_dwordx4 v[170:171], off
	s_mulk_i32 s17, 0x3000
	ds_read_b128 v[194:197], v140 offset:6144
	v_mfma_f32_32x32x16_bf16 v[52:67], v[198:201], v[132:135], v[52:67]
	ds_read_b128 v[198:201], v140 offset:6656
	v_exp_f32_e32 v92, v92
	v_exp_f32_e32 v93, v93
	v_exp_f32_e32 v94, v94
	v_exp_f32_e32 v95, v95
	s_waitcnt lgkmcnt(0)
	v_mfma_f32_32x32x16_bf16 v[68:83], v[202:205], v[128:131], v[68:83]
	ds_read_b128 v[202:205], v140 offset:8192
	v_exp_f32_e32 v96, v96
	v_exp_f32_e32 v97, v97
	v_exp_f32_e32 v98, v98
	v_exp_f32_e32 v99, v99
	v_mfma_f32_32x32x16_bf16 v[52:67], v[190:193], v[128:131], v[52:67]
	ds_read_b128 v[190:193], v140 offset:8704
	v_add_f32_e32 v147, v100, v101
	ds_read_b64_tr_b16 v[172:173], v141 offset:49152
	ds_read_b64_tr_b16 v[174:175], v141 offset:49664
	v_add_f32_e32 v146, v102, v147
	v_add_f32_e32 v146, v103, v146
	v_add_f32_e32 v146, v104, v146
	v_add_f32_e32 v144, v105, v146
	v_cvt_pk_bf16_f32 v156, v100, v101
	v_mfma_f32_32x32x16_bf16 v[68:83], v[194:197], v[124:127], v[68:83]
	ds_read_b128 v[194:197], v140 offset:10240
	v_cvt_pk_bf16_f32 v157, v102, v103
	ds_read_b64_tr_b16 v[100:101], v141 offset:53248
	ds_read_b64_tr_b16 v[102:103], v141 offset:53760
	v_add_f32_e32 v144, v106, v144
	v_add_f32_e32 v144, v107, v144
	v_add_f32_e32 v144, v108, v144
	v_add_f32_e32 v144, v109, v144
	v_cvt_pk_bf16_f32 v158, v104, v105
	v_mfma_f32_32x32x16_bf16 v[52:67], v[198:201], v[124:127], v[52:67]
	ds_read_b128 v[198:201], v140 offset:10752
	v_cvt_pk_bf16_f32 v159, v106, v107
	ds_read_b64_tr_b16 v[104:105], v141 offset:50176
	ds_read_b64_tr_b16 v[106:107], v141 offset:50688
	v_add_f32_e32 v144, v110, v144
	v_add_f32_e32 v144, v111, v144
	v_add_f32_e32 v144, v112, v144
	v_add_f32_e32 v144, v113, v144
	v_cvt_pk_bf16_f32 v160, v108, v109
	s_waitcnt lgkmcnt(0)
	v_mfma_f32_32x32x16_bf16 v[68:83], v[202:205], v[120:123], v[68:83]
	v_cvt_pk_bf16_f32 v161, v110, v111
	ds_read_b64_tr_b16 v[108:109], v141 offset:54272
	ds_read_b64_tr_b16 v[110:111], v141 offset:54784
	v_add_f32_e32 v144, v114, v144
	v_add_f32_e32 v144, v115, v144
	v_add_f32_e32 v144, v84, v144
	v_add_f32_e32 v144, v85, v144
	v_cvt_pk_bf16_f32 v162, v112, v113
	v_cvt_pk_bf16_f32 v163, v114, v115
	ds_read_b64_tr_b16 v[112:113], v141 offset:51200
	v_mfma_f32_32x32x16_bf16 v[52:67], v[190:193], v[120:123], v[52:67]
	ds_read_b64_tr_b16 v[114:115], v141 offset:51712
	v_add_f32_e32 v144, v86, v144
	v_add_f32_e32 v144, v87, v144
	v_add_f32_e32 v144, v88, v144
	v_add_f32_e32 v144, v89, v144
	v_cvt_pk_bf16_f32 v164, v84, v85
	v_cvt_pk_bf16_f32 v165, v86, v87
	ds_read_b64_tr_b16 v[84:85], v141 offset:55296
	ds_read_b64_tr_b16 v[86:87], v141 offset:55808
	v_add_f32_e32 v144, v90, v144
	v_mfma_f32_32x32x16_bf16 v[68:83], v[194:197], v[116:119], v[68:83]
	v_add_f32_e32 v144, v91, v144
	v_add_f32_e32 v144, v92, v144
	v_add_f32_e32 v144, v93, v144
	v_cvt_pk_bf16_f32 v166, v88, v89
	v_cvt_pk_bf16_f32 v167, v90, v91
	ds_read_b64_tr_b16 v[88:89], v141 offset:52224
	ds_read_b64_tr_b16 v[90:91], v141 offset:52736
	v_add_f32_e32 v144, v94, v144
	v_add_f32_e32 v144, v95, v144
	v_add_f32_e32 v144, v96, v144
	v_mfma_f32_32x32x16_bf16 v[52:67], v[198:201], v[116:119], v[52:67]
	v_add_f32_e32 v144, v97, v144
	v_cvt_pk_bf16_f32 v168, v92, v93
	v_cvt_pk_bf16_f32 v169, v94, v95
	ds_read_b64_tr_b16 v[92:93], v141 offset:56320
	ds_read_b64_tr_b16 v[94:95], v141 offset:56832
	v_add_f32_e32 v140, v98, v144
	v_add_f32_e32 v140, v99, v140
	v_cvt_pk_bf16_f32 v170, v96, v97
	v_cvt_pk_bf16_f32 v171, v98, v99
	s_setprio 0
	s_cmp_lt_i32 s27, s52
	s_cbranch_scc0 .LBB0_1171

.LBB0_1163:
	s_waitcnt lgkmcnt(0)
	v_mfma_f32_32x32x16_bf16 v[4:19], v[156:159], v[172:175], v[4:19]
	v_exp_f32_e32 v68, v68
	v_exp_f32_e32 v69, v69
	v_exp_f32_e32 v70, v70
	v_exp_f32_e32 v71, v71
	v_mfma_f32_32x32x16_bf16 v[20:35], v[156:159], v[100:103], v[20:35]
	v_exp_f32_e32 v72, v72
	v_exp_f32_e32 v73, v73
	v_exp_f32_e32 v74, v74
	v_exp_f32_e32 v75, v75
	s_add_i32 s12, s16, -1
	s_and_b32 s12, s12, 3
	s_mulk_i32 s12, 0x3000
	v_add_u32_e32 v156, s12, v188
	s_add_i32 s12, s14, 0x4000
	s_and_b32 s12, s12, 0x6000
	v_add_u32_e32 v157, s12, v186
	ds_read_b128 v[202:205], v156
	ds_read_b128 v[190:193], v156 offset:512
	ds_read_b128 v[194:197], v156 offset:2048
	ds_read_b128 v[198:201], v156 offset:2560
	v_mfma_f32_32x32x16_bf16 v[4:19], v[160:163], v[104:107], v[4:19]
	v_exp_f32_e32 v76, v76
	v_exp_f32_e32 v77, v77
	v_exp_f32_e32 v78, v78
	v_exp_f32_e32 v79, v79
	v_mfma_f32_32x32x16_bf16 v[20:35], v[160:163], v[108:111], v[20:35]
	v_exp_f32_e32 v80, v80
	v_exp_f32_e32 v81, v81
	v_exp_f32_e32 v82, v82
	v_exp_f32_e32 v83, v83
	v_mfma_f32_32x32x16_bf16 v[4:19], v[164:167], v[112:115], v[4:19]
	v_exp_f32_e32 v52, v52
	v_exp_f32_e32 v53, v53
	v_exp_f32_e32 v54, v54
	v_exp_f32_e32 v55, v55
	v_mfma_f32_32x32x16_bf16 v[20:35], v[164:167], v[84:87], v[20:35]
	v_exp_f32_e32 v56, v56
	v_exp_f32_e32 v57, v57
	v_exp_f32_e32 v58, v58
	v_exp_f32_e32 v59, v59
	v_mfma_f32_32x32x16_bf16 v[4:19], v[168:171], v[88:91], v[4:19]
	v_mfma_f32_32x32x16_bf16 v[20:35], v[168:171], v[92:95], v[20:35]
	s_and_b64 vcc, exec, s[10:11]
	s_cbranch_vccnz .Lmla_resc2
